# sleep+s_wakeup barriers for LSTM and worker waves (last arriver pings), on top of grid-barrier poll rewrite and L1 ds_read hoist
# speedup vs baseline: 1.0150x; 1.0026x over previous
.LBB1_15:
	ds_read_b32 v3, v1
	s_mov_b64 s[4:5], -1
	s_waitcnt lgkmcnt(0)
	v_readfirstlane_b32 s3, v3
	s_cmp_gt_i32 s3, 3
	s_cbranch_scc1 .LBB1_14
	s_mov_b64 s[4:5], 0
	s_sleep 20
	s_branch .LBB1_14
.LBB1_17:
	s_wakeup
	s_setprio 3
	s_mul_i32 s6, s2, 0x2800
	s_mul_hi_i32 s3, s2, 0x2800
	s_add_u32 s4, s54, s6
	v_mov_b32_e32 v1, 0
	s_addc_u32 s5, s55, s3
	v_lshlrev_b32_e32 v4, 2, v0
	v_mov_b32_e32 v5, v1
	s_movk_i32 s7, 0x1000
	v_lshl_add_u64 v[8:9], s[4:5], 0, v[4:5]
	v_or_b32_e32 v3, 0x1000, v4
	v_add_co_u32_e32 v28, vcc, s7, v8
	global_load_dword v26, v4, s[4:5] offset:-3072
	global_load_dword v24, v4, s[4:5] offset:-2048
	global_load_dword v22, v4, s[4:5] offset:-1024
	global_load_dword v20, v4, s[4:5]
	global_load_dword v18, v4, s[4:5] offset:1024
	global_load_dword v16, v4, s[4:5] offset:2048
	global_load_dword v12, v3, s[4:5]
	global_load_dword v14, v4, s[4:5] offset:3072
	v_addc_co_u32_e32 v29, vcc, 0, v9, vcc
	global_load_dword v10, v[28:29], off offset:1024
	s_add_u32 s4, s52, s6
	s_addc_u32 s5, s53, s3
	v_lshl_add_u64 v[32:33], s[4:5], 0, v[4:5]
	global_load_dword v31, v4, s[4:5] offset:-3072
	global_load_dword v8, v[28:29], off offset:2048
	global_load_dword v30, v4, s[4:5] offset:-2048
	global_load_dword v27, v4, s[4:5] offset:-1024
	global_load_dword v25, v4, s[4:5]
	global_load_dword v23, v4, s[4:5] offset:1024
	global_load_dword v21, v4, s[4:5] offset:2048
	global_load_dword v19, v4, s[4:5] offset:3072
	global_load_dword v17, v3, s[4:5]
	v_add_co_u32_e32 v4, vcc, s7, v32
	s_mov_b32 s3, 0x66666667
	s_nop 0
	v_addc_co_u32_e32 v5, vcc, 0, v33, vcc
	global_load_dword v15, v[4:5], off offset:1024
	global_load_dword v13, v[4:5], off offset:2048
	v_mov_b32_e32 v3, 0x1ef00
	v_mov_b32_e32 v4, 1
	s_waitcnt vmcnt(19)
	v_mul_hi_i32 v5, v26, s3
	s_waitcnt vmcnt(18)
	v_mul_hi_i32 v7, v24, s3
	v_lshrrev_b32_e32 v33, 31, v5
	v_ashrrev_i32_e32 v5, 5, v5
	s_waitcnt vmcnt(17)
	v_mul_hi_i32 v9, v22, s3
	v_lshrrev_b32_e32 v34, 31, v7
	v_ashrrev_i32_e32 v7, 5, v7
	v_add_u32_e32 v57, v5, v33
	s_waitcnt vmcnt(16)
	v_mul_hi_i32 v11, v20, s3
	s_waitcnt vmcnt(15)
	v_mul_hi_i32 v28, v18, s3
	s_waitcnt vmcnt(14)
	v_mul_hi_i32 v29, v16, s3
	s_waitcnt vmcnt(13)
	v_mul_hi_i32 v32, v12, s3
	v_lshrrev_b32_e32 v35, 31, v9
	v_ashrrev_i32_e32 v9, 5, v9
	v_add_u32_e32 v54, v7, v34
	s_waitcnt vmcnt(12)
	v_mul_hi_i32 v5, v14, s3
	v_lshl_add_u32 v60, v57, 2, v3
	v_lshrrev_b32_e32 v36, 31, v11
	v_ashrrev_i32_e32 v11, 5, v11
	v_lshrrev_b32_e32 v37, 31, v28
	v_ashrrev_i32_e32 v28, 5, v28
	v_lshrrev_b32_e32 v38, 31, v29
	v_ashrrev_i32_e32 v29, 5, v29
	v_lshrrev_b32_e32 v39, 31, v32
	v_ashrrev_i32_e32 v32, 5, v32
	v_add_u32_e32 v51, v9, v35
	s_waitcnt vmcnt(11)
	v_mul_hi_i32 v7, v10, s3
	v_lshl_add_u32 v58, v54, 2, v3
	v_lshrrev_b32_e32 v9, 31, v5
	v_ashrrev_i32_e32 v5, 5, v5
	ds_add_rtn_u32 v61, v60, v4
	v_add_u32_e32 v48, v11, v36
	v_add_u32_e32 v44, v28, v37
	v_add_u32_e32 v41, v29, v38
	v_add_u32_e32 v32, v32, v39
	v_lshl_add_u32 v55, v51, 2, v3
	v_lshrrev_b32_e32 v11, 31, v7
	v_add_u32_e32 v42, v5, v9
	ds_add_rtn_u32 v59, v58, v4
	v_ashrrev_i32_e32 v5, 5, v7
	v_lshl_add_u32 v52, v48, 2, v3
	v_lshl_add_u32 v49, v44, 2, v3
	v_lshl_add_u32 v46, v41, 2, v3
	v_lshl_add_u32 v38, v32, 2, v3
	v_lshl_add_u32 v45, v42, 2, v3
	ds_add_rtn_u32 v56, v55, v4
	ds_add_rtn_u32 v53, v52, v4
	ds_add_rtn_u32 v50, v49, v4
	ds_add_rtn_u32 v47, v46, v4
	ds_add_rtn_u32 v43, v45, v4
	ds_add_rtn_u32 v40, v38, v4
	v_add_u32_e32 v35, v5, v11
	s_waitcnt vmcnt(9)
	v_mul_hi_i32 v5, v8, s3
	v_lshrrev_b32_e32 v7, 31, v5
	v_ashrrev_i32_e32 v5, 5, v5
	v_lshl_add_u32 v39, v35, 2, v3
	v_add_u32_e32 v33, v5, v7
	ds_add_rtn_u32 v36, v39, v4
	v_lshl_add_u32 v37, v33, 2, v3
	ds_add_rtn_u32 v34, v37, v4
	s_waitcnt lgkmcnt(0)
	s_and_saveexec_b64 s[4:5], s[20:21]
	s_cbranch_execz .LBB1_20
	s_mov_b64 s[6:7], exec
	v_mbcnt_lo_u32_b32 v3, s6, 0
	v_mbcnt_hi_u32_b32 v3, s7, v3
	v_cmp_eq_u32_e32 vcc, 0, v3
	s_and_b64 s[8:9], exec, vcc
	s_mov_b64 exec, s[8:9]
	s_bcnt1_i32_b64 s3, s[6:7]
	v_mov_b32_e32 v3, 0x20e24
	v_mov_b32_e32 v4, s3
	ds_add_u32 v3, v4

.LBB1_22:
	ds_read_b32 v4, v3
	s_mov_b64 s[4:5], -1
	s_waitcnt lgkmcnt(0)
	v_readfirstlane_b32 s3, v4
	s_cmp_gt_i32 s3, 7
	s_cbranch_scc1 .LBB1_21
	s_mov_b64 s[4:5], 0
	s_sleep 20
	s_branch .LBB1_21
.LBB1_24:
	s_wakeup
	s_setprio 3
	ds_read_b32 v65, v2
	s_movk_i32 s3, 0x3fa
	v_cmp_gt_u32_e64 s[18:19], s3, v0
	s_waitcnt lgkmcnt(0)
	v_cmp_lt_i32_e64 s[16:17], 0, v65
	s_and_b64 s[6:7], s[18:19], s[16:17]
	s_and_saveexec_b64 s[4:5], s[6:7]
	s_cbranch_execz .LBB1_26
	v_lshlrev_b32_e32 v2, 2, v0
	global_atomic_add v2, v65, s[42:43] offset:-3072

.LBB1_78:
	ds_read_b32 v3, v2
	s_mov_b64 s[4:5], -1
	s_waitcnt lgkmcnt(0)
	v_readfirstlane_b32 s3, v3
	s_cmp_gt_i32 s3, 11
	s_cbranch_scc1 .LBB1_77
	s_mov_b64 s[4:5], 0
	s_sleep 20
	s_branch .LBB1_77
.LBB1_80:
	s_wakeup
	s_setprio 3
	v_cmp_eq_u32_e64 s[4:5], 0, v6
	s_and_saveexec_b64 s[6:7], s[4:5]
	s_cbranch_execz .LBB1_104
	s_mov_b64 s[10:11], exec
	v_mbcnt_lo_u32_b32 v2, s10, 0
	v_mbcnt_hi_u32_b32 v2, s11, v2
	v_cmp_eq_u32_e32 vcc, 0, v2
	s_and_saveexec_b64 s[8:9], vcc
	s_cbranch_execz .LBB1_83
	s_bcnt1_i32_b64 s3, s[10:11]
	v_mov_b32_e32 v2, 0
	v_mov_b32_e32 v3, s3
	global_atomic_add v2, v3, s[42:43] offset:2048

.LBB1_109:
	ds_read_b32 v3, v2
	s_mov_b64 s[6:7], -1
	s_waitcnt lgkmcnt(0)
	v_readfirstlane_b32 s3, v3
	s_cmp_gt_i32 s3, 15
	s_cbranch_scc1 .LBB1_108
	s_mov_b64 s[6:7], 0
	s_sleep 20
	s_branch .LBB1_108
.LBB1_111:
	s_wakeup
	s_setprio 3
	v_mov_b32_e32 v2, 0x202dc
	ds_read_b32 v2, v2
	s_waitcnt lgkmcnt(0)
	v_cmp_eq_u32_e32 vcc, 0, v2
	s_cbranch_vccnz .LBB1_363
	v_mov_b32_e32 v2, 0
	s_and_saveexec_b64 s[6:7], s[18:19]
	s_cbranch_execz .LBB1_114
	v_lshlrev_b32_e32 v2, 2, v0
	global_load_dword v2, v2, s[42:43] offset:-3072 sc1

.LBB1_125:
	ds_read_b32 v65, v5
	s_mov_b64 s[16:17], -1
	s_waitcnt lgkmcnt(0)
	v_readfirstlane_b32 s3, v65
	s_cmp_gt_i32 s3, 19
	s_cbranch_scc1 .LBB1_124
	s_mov_b64 s[16:17], 0
	s_sleep 20
	s_branch .LBB1_124
.LBB1_127:
	s_wakeup
	s_setprio 3
	v_mov_b32_e32 v65, 0
	v_cmp_lt_i32_e32 vcc, 0, v4
	s_and_saveexec_b64 s[16:17], vcc
	s_cbranch_execz .LBB1_137
	v_cmp_lt_u32_e32 vcc, 3, v4
	s_mov_b64 s[34:35], -1
	v_mov_b32_e32 v5, 0
	v_mov_b32_e32 v65, 0
	s_and_saveexec_b64 s[18:19], vcc
	s_cbranch_execz .LBB1_132
	v_and_b32_e32 v5, 0x7ffffffc, v4
	s_mov_b32 s3, 0x202c8
	s_mov_b64 s[34:35], 0
	v_mov_b32_e32 v68, 0
	v_mov_b32_e32 v65, 0
	v_mov_b32_e32 v70, 0
	v_mov_b32_e32 v69, 0
	v_mov_b32_e32 v71, v5

.LBB1_142:
	ds_read_b32 v3, v2
	s_mov_b64 s[16:17], -1
	s_waitcnt lgkmcnt(0)
	v_readfirstlane_b32 s3, v3
	s_cmp_gt_i32 s3, 23
	s_cbranch_scc1 .LBB1_141
	s_mov_b64 s[16:17], 0
	s_sleep 20
	s_branch .LBB1_141
.LBB1_144:
	s_wakeup
	s_setprio 3
	ds_read2st64_b32 v[2:3], v60 offset0:4 offset1:8
	s_mov_b32 s3, 0xffb0
	v_mad_u64_u32 v[4:5], s[16:17], v57, s3, v[26:27]
	v_lshl_or_b32 v4, v4, 16, v31
	s_waitcnt lgkmcnt(0)
	v_add3_u32 v2, v2, v61, v3
	v_ashrrev_i32_e32 v3, 31, v2
	v_lshl_add_u64 v[2:3], v[2:3], 2, s[44:45]
	global_store_dword v[2:3], v4, off sc1
	ds_read2st64_b32 v[2:3], v58 offset0:4 offset1:8
	v_mad_u64_u32 v[4:5], s[16:17], v54, s3, v[24:25]
	v_lshl_or_b32 v4, v4, 16, v30
	s_waitcnt lgkmcnt(0)
	v_add3_u32 v2, v2, v59, v3
	v_ashrrev_i32_e32 v3, 31, v2
	v_lshl_add_u64 v[2:3], v[2:3], 2, s[44:45]
	global_store_dword v[2:3], v4, off sc1
	ds_read2st64_b32 v[2:3], v55 offset0:4 offset1:8
	v_mad_u64_u32 v[4:5], s[16:17], v51, s3, v[22:23]
	v_lshl_or_b32 v4, v4, 16, v27
	s_waitcnt lgkmcnt(0)
	v_add3_u32 v2, v2, v56, v3
	v_ashrrev_i32_e32 v3, 31, v2
	v_lshl_add_u64 v[2:3], v[2:3], 2, s[44:45]
	global_store_dword v[2:3], v4, off sc1
	ds_read2st64_b32 v[2:3], v52 offset0:4 offset1:8
	v_mad_u64_u32 v[4:5], s[16:17], v48, s3, v[20:21]
	v_lshl_or_b32 v4, v4, 16, v25
	s_waitcnt lgkmcnt(0)
	v_add3_u32 v2, v2, v53, v3
	v_ashrrev_i32_e32 v3, 31, v2
	v_lshl_add_u64 v[2:3], v[2:3], 2, s[44:45]
	global_store_dword v[2:3], v4, off sc1
	ds_read2st64_b32 v[2:3], v49 offset0:4 offset1:8
	v_mad_u64_u32 v[4:5], s[16:17], v44, s3, v[18:19]
	v_lshl_or_b32 v4, v4, 16, v23
	s_waitcnt lgkmcnt(0)
	v_add3_u32 v2, v2, v50, v3
	v_ashrrev_i32_e32 v3, 31, v2
	v_lshl_add_u64 v[2:3], v[2:3], 2, s[44:45]
	global_store_dword v[2:3], v4, off sc1
	ds_read2st64_b32 v[2:3], v46 offset0:4 offset1:8
	v_mad_u64_u32 v[4:5], s[16:17], v41, s3, v[16:17]
	v_lshl_or_b32 v4, v4, 16, v21
	s_waitcnt lgkmcnt(0)
	v_add3_u32 v2, v2, v47, v3
	v_ashrrev_i32_e32 v3, 31, v2
	v_lshl_add_u64 v[2:3], v[2:3], 2, s[44:45]
	global_store_dword v[2:3], v4, off sc1
	ds_read2st64_b32 v[2:3], v45 offset0:4 offset1:8
	v_mad_u64_u32 v[4:5], s[16:17], v42, s3, v[14:15]
	v_lshl_or_b32 v4, v4, 16, v19
	s_waitcnt lgkmcnt(0)
	v_add3_u32 v2, v2, v43, v3
	v_ashrrev_i32_e32 v3, 31, v2
	v_lshl_add_u64 v[2:3], v[2:3], 2, s[44:45]
	global_store_dword v[2:3], v4, off sc1
	ds_read2st64_b32 v[2:3], v38 offset0:4 offset1:8
	v_mad_u64_u32 v[4:5], s[16:17], v32, s3, v[12:13]
	v_lshl_or_b32 v4, v4, 16, v17
	s_waitcnt lgkmcnt(0)
	v_add3_u32 v2, v2, v40, v3
	v_ashrrev_i32_e32 v3, 31, v2
	v_lshl_add_u64 v[2:3], v[2:3], 2, s[44:45]
	global_store_dword v[2:3], v4, off sc1
	ds_read2st64_b32 v[2:3], v39 offset0:4 offset1:8
	v_mad_u64_u32 v[4:5], s[16:17], v35, s3, v[10:11]
	v_lshl_or_b32 v4, v4, 16, v15
	s_waitcnt lgkmcnt(0)
	v_add3_u32 v2, v2, v36, v3
	v_ashrrev_i32_e32 v3, 31, v2
	v_lshl_add_u64 v[2:3], v[2:3], 2, s[44:45]
	global_store_dword v[2:3], v4, off sc1
	ds_read2st64_b32 v[2:3], v37 offset0:4 offset1:8
	v_mad_u64_u32 v[4:5], s[16:17], v33, s3, v[8:9]
	v_lshl_or_b32 v4, v4, 16, v13
	s_waitcnt lgkmcnt(0)
	v_add3_u32 v2, v2, v34, v3
	v_ashrrev_i32_e32 v3, 31, v2
	v_lshl_add_u64 v[2:3], v[2:3], 2, s[44:45]
	global_store_dword v[2:3], v4, off sc1
	s_waitcnt vmcnt(0)
	s_and_saveexec_b64 s[16:17], s[20:21]
	s_cbranch_execz .LBB1_147
	s_mov_b64 s[18:19], exec
	v_mbcnt_lo_u32_b32 v2, s18, 0
	v_mbcnt_hi_u32_b32 v2, s19, v2
	v_cmp_eq_u32_e32 vcc, 0, v2
	s_and_b64 s[34:35], exec, vcc
	s_mov_b64 exec, s[34:35]
	s_bcnt1_i32_b64 s3, s[18:19]
	v_mov_b32_e32 v2, 0x20e24
	v_mov_b32_e32 v3, s3
	ds_add_u32 v2, v3

.LBB1_149:
	ds_read_b32 v3, v2
	s_mov_b64 s[16:17], -1
	s_waitcnt lgkmcnt(0)
	v_readfirstlane_b32 s3, v3
	s_cmp_gt_i32 s3, 27
	s_cbranch_scc1 .LBB1_148
	s_mov_b64 s[16:17], 0
	s_sleep 20
	s_branch .LBB1_148
.LBB1_151:
	s_wakeup
	s_setprio 3
	s_and_saveexec_b64 s[16:17], s[4:5]
	s_cbranch_execz .LBB1_176
	s_mov_b64 s[34:35], exec
	v_mbcnt_lo_u32_b32 v2, s34, 0
	v_mbcnt_hi_u32_b32 v2, s35, v2
	v_cmp_eq_u32_e32 vcc, 0, v2
	s_and_saveexec_b64 s[18:19], vcc
	s_cbranch_execz .LBB1_154
	s_bcnt1_i32_b64 s3, s[34:35]
	v_mov_b32_e32 v2, 0
	v_mov_b32_e32 v3, s3
	global_atomic_add v2, v3, s[42:43] offset:2304

.LBB1_181:
	ds_read_b32 v3, v2
	s_mov_b64 s[16:17], -1
	s_waitcnt lgkmcnt(0)
	v_readfirstlane_b32 s3, v3
	s_cmp_gt_i32 s3, 31
	s_cbranch_scc1 .LBB1_180
	s_mov_b64 s[16:17], 0
	s_sleep 20
	s_branch .LBB1_180
.LBB1_183:
	s_wakeup
	s_setprio 3
	v_mov_b32_e32 v2, 0x202dc
	ds_read_b32 v2, v2
	s_waitcnt lgkmcnt(0)
	v_cmp_eq_u32_e32 vcc, 0, v2
	s_cbranch_vccnz .LBB1_363
	s_lshl_b32 s3, s2, 2
	s_add_i32 s3, s3, 0x1ef00
	v_mov_b32_e32 v2, s3
	ds_read2st64_b32 v[2:3], v2 offset0:4 offset1:12
	s_movk_i32 s16, 0x350
	v_cmp_gt_u32_e64 s[16:17], s16, v0
	s_waitcnt lgkmcnt(0)
	v_readfirstlane_b32 s3, v3
	s_and_saveexec_b64 s[18:19], s[16:17]
	v_mov_b32_e32 v3, 0
	v_add_u32_e32 v4, 0x400, v28
	ds_write2_b32 v4, v3, v3 offset1:80
	s_or_b64 exec, exec, s[18:19]
	s_waitcnt lgkmcnt(0)
	s_and_saveexec_b64 s[18:19], s[20:21]
	s_cbranch_execz .LBB1_189
	s_mov_b64 s[34:35], exec
	v_mbcnt_lo_u32_b32 v3, s34, 0
	v_mbcnt_hi_u32_b32 v3, s35, v3
	v_cmp_eq_u32_e32 vcc, 0, v3
	s_and_b64 s[36:37], exec, vcc
	s_mov_b64 exec, s[36:37]
	s_bcnt1_i32_b64 s34, s[34:35]
	v_mov_b32_e32 v3, 0x20e24
	v_mov_b32_e32 v4, s34
	ds_add_u32 v3, v4

.LBB1_191:
	ds_read_b32 v4, v3
	s_waitcnt lgkmcnt(0)
	v_readfirstlane_b32 s18, v4
	s_cmp_gt_i32 s18, 35
	s_mov_b64 s[18:19], -1
	s_cbranch_scc1 .LBB1_190
	s_mov_b64 s[18:19], 0
	s_sleep 20
	s_branch .LBB1_190
.LBB1_193:
	s_wakeup
	s_setprio 3
	s_cmp_gt_i32 s3, 0
	s_mov_b32 s38, 0
	s_cselect_b64 s[18:19], -1, 0
	s_cmp_lt_i32 s3, 1
	v_ashrrev_i32_e32 v3, 31, v2
	v_add_u32_e32 v8, v0, v2
	s_cbranch_scc1 .LBB1_212
	v_lshl_add_u64 v[4:5], v[2:3], 0, v[0:1]
	s_movk_i32 s34, 0xfc00
	v_lshl_add_u64 v[4:5], v[4:5], 2, s[44:45]
	s_mov_b32 s35, -1
	v_lshl_add_u64 v[4:5], v[4:5], 0, s[34:35]
	v_mov_b32_e32 v10, 1
	s_mov_b64 s[34:35], 0x1000
	v_mov_b32_e32 v12, 0x1ff00
	s_branch .LBB1_196

.LBB1_217:
	ds_read_b32 v5, v4
	s_waitcnt lgkmcnt(0)
	v_readfirstlane_b32 s34, v5
	s_cmp_gt_i32 s34, 39
	s_mov_b64 s[34:35], -1
	s_cbranch_scc1 .LBB1_216
	s_mov_b64 s[34:35], 0
	s_sleep 20
	s_branch .LBB1_216
.LBB1_219:
	s_wakeup
	s_setprio 3
	v_cmp_gt_u32_e32 vcc, 64, v6
	s_and_saveexec_b64 s[34:35], vcc
	s_cbranch_execz .LBB1_224
	v_lshlrev_b32_e32 v10, 2, v106
	v_or_b32_e32 v4, 0x1ff00, v10
	ds_read_b32 v12, v4
	v_bfrev_b32_e32 v13, 0.5
	v_add_u32_e32 v10, 0x20180, v10
	s_waitcnt lgkmcnt(0)
	ds_bpermute_b32 v4, v29, v12
	s_waitcnt lgkmcnt(0)
	v_cndmask_b32_e64 v4, v4, 0, s[20:21]
	v_add_u32_e32 v4, v4, v12
	ds_bpermute_b32 v5, v62, v4
	s_waitcnt lgkmcnt(0)
	v_cndmask_b32_e64 v5, v5, 0, s[6:7]
	v_add_u32_e32 v4, v5, v4
	ds_bpermute_b32 v5, v63, v4
	s_waitcnt lgkmcnt(0)
	v_cndmask_b32_e64 v5, v5, 0, s[10:11]
	v_add_u32_e32 v4, v5, v4
	ds_bpermute_b32 v5, v64, v4
	s_waitcnt lgkmcnt(0)
	v_cndmask_b32_e64 v5, v5, 0, s[8:9]
	v_add_u32_e32 v4, v5, v4
	ds_bpermute_b32 v5, v66, v4
	s_waitcnt lgkmcnt(0)
	v_cndmask_b32_e64 v5, v5, 0, s[12:13]
	v_add_u32_e32 v4, v5, v4
	ds_bpermute_b32 v5, v67, v4
	s_waitcnt lgkmcnt(0)
	v_cndmask_b32_e64 v5, v5, 0, s[14:15]
	v_add_u32_e32 v14, v5, v4
	v_lshl_or_b32 v4, v9, 2, v13
	ds_bpermute_b32 v4, v4, v14
	v_mov_b32_e32 v5, 0
	v_sub_u32_e32 v12, v14, v12
	ds_write_b32 v10, v12
	s_and_saveexec_b64 s[14:15], s[12:13]
	ds_read_b32 v5, v28 offset:1280
	s_or_b64 exec, exec, s[14:15]
	s_waitcnt lgkmcnt(0)
	ds_bpermute_b32 v10, v29, v5
	s_waitcnt lgkmcnt(0)
	v_cndmask_b32_e64 v10, v10, 0, s[20:21]
	v_add_u32_e32 v10, v10, v5
	ds_bpermute_b32 v12, v62, v10
	s_waitcnt lgkmcnt(0)
	v_cndmask_b32_e64 v12, v12, 0, s[6:7]
	v_add_u32_e32 v10, v12, v10
	ds_bpermute_b32 v12, v63, v10
	s_waitcnt lgkmcnt(0)
	v_cndmask_b32_e64 v12, v12, 0, s[10:11]
	v_add_u32_e32 v10, v12, v10
	ds_bpermute_b32 v12, v64, v10
	s_and_b64 exec, exec, s[12:13]
	s_cbranch_execz .LBB1_224
	s_waitcnt lgkmcnt(0)
	v_cndmask_b32_e64 v12, v12, 0, s[8:9]
	v_sub_u32_e32 v4, v4, v5
	v_add3_u32 v4, v4, v10, v12
	ds_write_b32 v28, v4 offset:1920

.LBB1_229:
	ds_read_b32 v5, v4
	s_waitcnt lgkmcnt(0)
	v_readfirstlane_b32 s6, v5
	s_cmp_gt_i32 s6, 43
	s_mov_b64 s[6:7], -1
	s_cbranch_scc1 .LBB1_228
	s_mov_b64 s[6:7], 0
	s_sleep 20
	s_branch .LBB1_228
.LBB1_231:
	s_wakeup
	s_setprio 3
	s_and_saveexec_b64 s[6:7], s[16:17]
	s_cbranch_execnz .LBB1_234
	s_or_b64 exec, exec, s[6:7]
	s_and_saveexec_b64 s[6:7], s[4:5]
	s_cbranch_execnz .LBB1_235

.LBB1_259:
	ds_read_b32 v2, v1
	s_mov_b64 s[6:7], -1
	s_waitcnt lgkmcnt(0)
	v_readfirstlane_b32 s3, v2
	s_cmp_gt_i32 s3, 47
	s_cbranch_scc1 .LBB1_258
	s_mov_b64 s[6:7], 0
	s_sleep 20
	s_branch .LBB1_258
.LBB1_261:
	s_wakeup
	s_setprio 3
	v_and_b32_e32 v1, 7, v0
	v_lshlrev_b32_e32 v2, 4, v1
	v_mov_b32_e32 v3, 0
	v_lshl_add_u64 v[16:17], s[24:25], 0, v[2:3]
	v_lshlrev_b32_e32 v2, 5, v1
	v_lshl_add_u64 v[2:3], s[56:57], 0, v[2:3]
	v_or_b32_e32 v4, 0xfffffc00, v0
	s_mov_b64 s[6:7], 0
	v_mov_b32_e32 v5, 0x20ce0
	s_movk_i32 s3, 0x108
	s_movk_i32 s8, 0x17f

.LBB1_272:
	ds_read_b32 v3, v2
	s_waitcnt lgkmcnt(0)
	v_readfirstlane_b32 s2, v3
	s_cmp_gt_i32 s2, 51
	s_mov_b64 s[2:3], -1
	s_cbranch_scc1 .LBB1_271
	s_mov_b64 s[2:3], 0
	s_sleep 20
	s_branch .LBB1_271
.LBB1_274:
	s_wakeup
	s_setprio 3
	s_and_saveexec_b64 s[2:3], s[4:5]
	s_cbranch_execz .LBB1_299
	s_mov_b64 s[6:7], exec
	v_mbcnt_lo_u32_b32 v2, s6, 0
	v_mbcnt_hi_u32_b32 v2, s7, v2
	v_cmp_eq_u32_e32 vcc, 0, v2
	s_and_saveexec_b64 s[4:5], vcc
	s_cbranch_execz .LBB1_277
	s_bcnt1_i32_b64 s6, s[6:7]
	v_mov_b32_e32 v2, 0
	v_mov_b32_e32 v3, s6
	global_atomic_add v2, v3, s[42:43] offset:2560

.LBB1_304:
	ds_read_b32 v3, v2
	s_waitcnt lgkmcnt(0)
	v_readfirstlane_b32 s2, v3
	s_cmp_gt_i32 s2, 55
	s_mov_b64 s[2:3], -1
	s_cbranch_scc1 .LBB1_303
	s_mov_b64 s[2:3], 0
	s_sleep 20
	s_branch .LBB1_303
.LBB1_306:
	s_wakeup
	s_setprio 3
	v_mov_b32_e32 v2, 0x202dc
	ds_read_b32 v2, v2
	s_waitcnt lgkmcnt(0)
	v_cmp_eq_u32_e32 vcc, 0, v2
	s_cbranch_vccnz .LBB1_363
	v_readfirstlane_b32 s2, v6
	s_ashr_i32 s4, s2, 6
	s_setprio 3
	s_cmp_gt_i32 s4, 9
	s_cbranch_scc1 .LBB1_353
	v_xor_b32_e32 v2, 32, v9
	v_add_u32_e32 v3, 64, v11
	v_cmp_lt_i32_e32 vcc, v2, v3
	s_mul_i32 s5, s4, 0x2800
	s_add_i32 s5, s5, 0xa000
	v_cndmask_b32_e32 v2, v9, v2, vcc
	v_lshlrev_b32_e32 v11, 2, v2
	v_xor_b32_e32 v2, 16, v9
	v_cmp_lt_i32_e32 vcc, v2, v3
	v_lshrrev_b32_e32 v19, 3, v106
	s_add_i32 s6, s5, 0x400
	v_cndmask_b32_e32 v2, v9, v2, vcc
	v_lshlrev_b32_e32 v21, 2, v2
	v_xor_b32_e32 v2, 8, v9
	v_cmp_lt_i32_e32 vcc, v2, v3
	v_mov_b32_e32 v3, 0x1c200
	v_lshl_or_b32 v18, v1, 4, v3
	v_cndmask_b32_e32 v2, v9, v2, vcc
	v_lshlrev_b32_e32 v54, 2, v2
	v_lshlrev_b32_e32 v2, 4, v106
	s_add_i32 s7, s5, 0x800
	s_add_i32 s8, s5, 0xc00
	s_add_i32 s9, s5, 0x1000
	s_add_i32 s10, s5, 0x1400
	s_add_i32 s11, s5, 0x1800
	s_add_i32 s12, s5, 0x1c00
	s_add_i32 s13, s5, 0x2000
	s_add_i32 s14, s5, 0x2400
	v_add_u32_e32 v55, s5, v2
	s_movk_i32 s15, 0x90
	s_mov_b32 s16, s4
	s_branch .LBB1_310

.LBB1_358:
	ds_read_b32 v27, v26
	s_waitcnt lgkmcnt(0)
	v_readfirstlane_b32 s4, v27
	s_cmp_gt_i32 s4, 59
	s_mov_b64 s[4:5], -1
	s_cbranch_scc1 .LBB1_357
	s_mov_b64 s[4:5], 0
	s_sleep 20
	s_branch .LBB1_357
.LBB1_360:
	s_wakeup
	v_and_b32_e32 v28, 15, v0
	s_setprio 3
	v_lshlrev_b32_e32 v26, 1, v1
	v_mov_b32_e32 v27, 0
	v_lshl_add_u64 v[26:27], s[26:27], 0, v[26:27]
	v_and_b32_e32 v29, 48, v0
	v_lshl_add_u64 v[26:27], s[2:3], 1, v[26:27]
	v_mul_u32_u24_e32 v1, 0x90, v28
	s_mov_b32 s2, 0x1c240
	v_add3_u32 v1, v1, v29, s2
	v_add_u32_e32 v28, s22, v28
	s_mov_b32 s2, 0

.LBB1_392:
	s_waitcnt lgkmcnt(0)
	s_mov_b64 exec, 1
	v_mov_b32_e32 v52, 1
	ds_add_rtn_u32 v52, v56, v52
	s_mov_b64 exec, -1
	s_add_i32 s9, s9, 1
	s_mul_i32 s10, s9, 12
	s_waitcnt lgkmcnt(0)
	v_readfirstlane_b32 s6, v52
	s_add_i32 s6, s6, 1
	s_cmp_ge_i32 s6, s10
	s_cbranch_scc1 .Lb1_last
	s_setprio 0
.Lb1_poll:
	s_sleep 60
	ds_read_b32 v52, v56
	s_waitcnt lgkmcnt(0)
	v_readfirstlane_b32 s6, v52
	s_cmp_ge_i32 s6, s10
	s_cbranch_scc0 .Lb1_poll
	s_branch .LBB1_370
.Lb1_last:
	s_wakeup
	s_branch .LBB1_370

.LBB1_427:
	s_waitcnt lgkmcnt(0)
	s_mov_b64 exec, 1
	v_mov_b32_e32 v70, 1
	ds_add_rtn_u32 v70, v75, v70
	s_mov_b64 exec, -1
	s_add_i32 s7, s7, 1
	s_mul_i32 s9, s7, 12
	s_waitcnt lgkmcnt(0)
	v_readfirstlane_b32 s10, v70
	s_add_i32 s10, s10, 1
	s_cmp_ge_i32 s10, s9
	s_cbranch_scc1 .Lb0_last
	s_setprio 0
.Lb0_poll:
	s_sleep 60
	ds_read_b32 v70, v75
	s_waitcnt lgkmcnt(0)
	v_readfirstlane_b32 s10, v70
	s_cmp_ge_i32 s10, s9
	s_cbranch_scc0 .Lb0_poll
	s_branch .LBB1_424
